# layer-2 N1 (adds the previous MoE output): route/slot words requested with the row, the eight expert-output loads issued together (7 serial memory round trips per row -> 2); on top of the combination
# speedup vs baseline: 1.0076x; 1.0076x over previous
.LBB0_399:
	v_readlane_b32 s40, v251, 5
	v_readlane_b32 s46, v251, 11
	v_readlane_b32 s47, v251, 12
	s_mov_b32 s0, 0xf800000
	s_mov_b32 s3, 0x42fe0000
	v_lshl_add_u64 v[68:69], s[46:47], 0, v[88:89]
	v_add_co_u32_e32 v106, vcc, 0x500000, v68
	v_readlane_b32 s41, v251, 6
	s_nop 0
	v_addc_co_u32_e32 v107, vcc, 0, v69, vcc
	v_lshl_add_u64 v[136:137], s[46:47], 0, v[84:85]
	v_lshl_add_u64 v[138:139], s[46:47], 0, v[86:87]
	global_load_dwordx4 v[130:133], v[136:137], off
	global_load_dwordx2 v[134:135], v[138:139], off
	global_load_dwordx2 v[68:69], v[106:107], off
	global_load_dwordx2 v[70:71], v[106:107], off offset:512
	global_load_dwordx2 v[98:99], v[106:107], off offset:1024
	global_load_dwordx2 v[112:113], v[106:107], off offset:1536
	v_readlane_b32 s42, v251, 7
	v_readlane_b32 s43, v251, 8
	v_readlane_b32 s44, v251, 9
	v_readlane_b32 s45, v251, 10
	s_waitcnt vmcnt(3)
	v_lshlrev_b32_e32 v108, 16, v68
	v_and_b32_e32 v109, 0xffff0000, v68
	v_lshlrev_b32_e32 v96, 16, v69
	v_and_b32_e32 v97, 0xffff0000, v69
	v_lshl_add_u64 v[68:69], s[46:47], 0, v[84:85]
	s_waitcnt vmcnt(2)
	v_lshlrev_b32_e32 v94, 16, v70
	v_and_b32_e32 v95, 0xffff0000, v70
	v_lshlrev_b32_e32 v110, 16, v71
	v_and_b32_e32 v111, 0xffff0000, v71
	s_waitcnt vmcnt(0)
	v_mov_b32_e32 v70, v132
	v_mov_b32_e32 v71, v133
	s_waitcnt vmcnt(0)
	v_lshl_add_u64 v[68:69], s[46:47], 0, v[86:87]
	v_mov_b32_e32 v68, v134
	v_mov_b32_e32 v69, v135
	v_lshlrev_b32_e32 v104, 16, v98
	v_and_b32_e32 v105, 0xffff0000, v98
	v_lshlrev_b32_e32 v102, 16, v99
	v_and_b32_e32 v103, 0xffff0000, v99
	v_lshlrev_b32_e32 v100, 16, v112
	v_and_b32_e32 v101, 0xffff0000, v112
	v_lshlrev_b32_e32 v98, 16, v113
	v_and_b32_e32 v99, 0xffff0000, v113
	v_mov_b32_e32 v128, v71
	s_waitcnt vmcnt(0)
	v_ashrrev_i32_e32 v113, 31, v68
	v_mov_b32_e32 v112, v68
	v_lshlrev_b64 v[112:113], 11, v[112:113]
	v_ashrrev_i32_e32 v115, 31, v69
	v_mov_b32_e32 v114, v69
	v_lshl_add_u64 v[112:113], v[82:83], 0, v[112:113]
	v_lshlrev_b64 v[68:69], 11, v[114:115]
	v_lshl_add_u64 v[114:115], v[82:83], 0, v[68:69]
	global_load_dwordx2 v[68:69], v[112:113], off
	global_load_dwordx2 v[122:123], v[114:115], off
	global_load_dwordx2 v[140:141], v[112:113], off offset:512
	global_load_dwordx2 v[142:143], v[114:115], off offset:512
	global_load_dwordx2 v[144:145], v[112:113], off offset:1024
	global_load_dwordx2 v[146:147], v[114:115], off offset:1024
	global_load_dwordx2 v[148:149], v[112:113], off offset:1536
	global_load_dwordx2 v[150:151], v[114:115], off offset:1536
	s_waitcnt vmcnt(7)
	v_lshlrev_b32_e32 v124, 16, v68
	s_waitcnt vmcnt(6)
	v_lshlrev_b32_e32 v126, 16, v122
	v_and_b32_e32 v127, 0xffff0000, v122
	v_lshlrev_b32_e32 v122, 16, v123
	v_and_b32_e32 v123, 0xffff0000, v123
	v_and_b32_e32 v125, 0xffff0000, v68
	v_lshlrev_b32_e32 v68, 16, v69
	v_and_b32_e32 v69, 0xffff0000, v69
	v_pk_mul_f32 v[122:123], v[128:129], v[122:123] op_sel_hi:[0,1]
	v_pk_mul_f32 v[126:127], v[128:129], v[126:127] op_sel_hi:[0,1]
	v_pk_fma_f32 v[124:125], v[70:71], v[124:125], v[126:127] op_sel_hi:[0,1,1]
	v_pk_fma_f32 v[68:69], v[70:71], v[68:69], v[122:123] op_sel_hi:[0,1,1]
	v_pk_fma_f32 v[96:97], v[64:65], v[68:69], v[96:97]
	v_pk_fma_f32 v[108:109], v[62:63], v[124:125], v[108:109]
	v_cvt_pk_bf16_f32 v69, v96, v97
	v_cvt_pk_bf16_f32 v68, v108, v109
	global_store_dwordx2 v[106:107], v[68:69], off
	s_waitcnt vmcnt(5)
	s_nop 0
	v_mov_b32_e32 v68, v140
	v_mov_b32_e32 v69, v141
	v_mov_b32_e32 v122, v142
	v_mov_b32_e32 v123, v143
	s_nop 0
	v_lshlrev_b32_e32 v124, 16, v68
	s_nop 0
	v_lshlrev_b32_e32 v126, 16, v122
	v_and_b32_e32 v127, 0xffff0000, v122
	v_lshlrev_b32_e32 v122, 16, v123
	v_and_b32_e32 v123, 0xffff0000, v123
	v_and_b32_e32 v125, 0xffff0000, v68
	v_lshlrev_b32_e32 v68, 16, v69
	v_and_b32_e32 v69, 0xffff0000, v69
	v_pk_mul_f32 v[122:123], v[128:129], v[122:123] op_sel_hi:[0,1]
	v_pk_mul_f32 v[126:127], v[128:129], v[126:127] op_sel_hi:[0,1]
	v_pk_fma_f32 v[124:125], v[70:71], v[124:125], v[126:127] op_sel_hi:[0,1,1]
	v_pk_fma_f32 v[68:69], v[70:71], v[68:69], v[122:123] op_sel_hi:[0,1,1]
	v_pk_fma_f32 v[68:69], v[56:57], v[68:69], v[110:111]
	v_pk_fma_f32 v[94:95], v[54:55], v[124:125], v[94:95]
	v_cvt_pk_bf16_f32 v111, v68, v69
	v_cvt_pk_bf16_f32 v110, v94, v95
	global_store_dwordx2 v[106:107], v[110:111], off offset:512
	s_waitcnt vmcnt(4)
	s_nop 0
	v_mov_b32_e32 v110, v144
	v_mov_b32_e32 v111, v145
	v_mov_b32_e32 v122, v146
	v_mov_b32_e32 v123, v147
	s_nop 0
	v_lshlrev_b32_e32 v124, 16, v110
	s_nop 0
	v_lshlrev_b32_e32 v126, 16, v122
	v_and_b32_e32 v127, 0xffff0000, v122
	v_lshlrev_b32_e32 v122, 16, v123
	v_and_b32_e32 v123, 0xffff0000, v123
	v_and_b32_e32 v125, 0xffff0000, v110
	v_lshlrev_b32_e32 v110, 16, v111
	v_and_b32_e32 v111, 0xffff0000, v111
	v_pk_mul_f32 v[122:123], v[128:129], v[122:123] op_sel_hi:[0,1]
	v_pk_mul_f32 v[126:127], v[128:129], v[126:127] op_sel_hi:[0,1]
	v_pk_fma_f32 v[124:125], v[70:71], v[124:125], v[126:127] op_sel_hi:[0,1,1]
	v_pk_fma_f32 v[110:111], v[70:71], v[110:111], v[122:123] op_sel_hi:[0,1,1]
	v_pk_fma_f32 v[102:103], v[52:53], v[110:111], v[102:103]
	v_pk_fma_f32 v[104:105], v[50:51], v[124:125], v[104:105]
	v_cvt_pk_bf16_f32 v111, v102, v103
	v_cvt_pk_bf16_f32 v110, v104, v105
	global_store_dwordx2 v[106:107], v[110:111], off offset:1024
	s_waitcnt vmcnt(3)
	s_nop 0
	v_mov_b32_e32 v110, v148
	v_mov_b32_e32 v111, v149
	v_mov_b32_e32 v112, v150
	v_mov_b32_e32 v113, v151
	s_nop 0
	v_lshlrev_b32_e32 v114, 16, v110
	s_nop 0
	v_lshlrev_b32_e32 v122, 16, v112
	v_and_b32_e32 v123, 0xffff0000, v112
	v_lshlrev_b32_e32 v112, 16, v113
	v_and_b32_e32 v113, 0xffff0000, v113
	v_and_b32_e32 v115, 0xffff0000, v110
	v_lshlrev_b32_e32 v110, 16, v111
	v_and_b32_e32 v111, 0xffff0000, v111
	v_pk_mul_f32 v[112:113], v[128:129], v[112:113] op_sel_hi:[0,1]
	v_pk_mul_f32 v[122:123], v[128:129], v[122:123] op_sel_hi:[0,1]
	v_pk_fma_f32 v[114:115], v[70:71], v[114:115], v[122:123] op_sel_hi:[0,1,1]
	v_pk_fma_f32 v[70:71], v[70:71], v[110:111], v[112:113] op_sel_hi:[0,1,1]
	v_pk_fma_f32 v[98:99], v[60:61], v[70:71], v[98:99]
	v_pk_fma_f32 v[100:101], v[58:59], v[114:115], v[100:101]
	v_cvt_pk_bf16_f32 v71, v98, v99
	v_cvt_pk_bf16_f32 v70, v100, v101
	global_store_dwordx2 v[106:107], v[70:71], off offset:1536
	v_pk_mul_f32 v[70:71], v[96:97], v[96:97]
	v_pk_mul_f32 v[106:107], v[108:109], v[108:109]
	s_nop 0
	v_pk_mov_b32 v[110:111], v[106:107], v[70:71] op_sel:[1,0]
	v_mov_b32_e32 v107, v71
	v_pk_add_f32 v[70:71], v[110:111], v[106:107]
	v_pk_mul_f32 v[106:107], v[68:69], v[68:69]
	v_pk_mul_f32 v[110:111], v[94:95], v[94:95]
	v_pk_add_f32 v[70:71], v[70:71], v[70:71] op_sel:[0,1] op_sel_hi:[1,0]
	v_pk_mov_b32 v[112:113], v[110:111], v[106:107] op_sel:[1,0]
	v_mov_b32_e32 v111, v107
	v_pk_add_f32 v[106:107], v[112:113], v[110:111]
	v_mul_f32_e32 v110, v100, v100
	v_mul_f32_e32 v111, v101, v101
	v_pk_add_f32 v[106:107], v[106:107], v[106:107] op_sel:[0,1] op_sel_hi:[1,0]
	v_mov_b32_e32 v71, v110
	v_mov_b32_e32 v107, v111
	v_pk_add_f32 v[70:71], v[70:71], v[106:107]
	v_mul_f32_e32 v106, v105, v105
	v_mul_f32_e32 v110, v103, v103
	v_mul_f32_e32 v112, v98, v98
	v_mul_f32_e32 v113, v99, v99
	v_pk_fma_f32 v[106:107], v[104:105], v[104:105], v[106:107] op_sel_hi:[1,1,0]
	v_pk_fma_f32 v[110:111], v[102:103], v[102:103], v[110:111] op_sel_hi:[1,1,0]
	v_mov_b32_e32 v107, v112
	v_mov_b32_e32 v111, v113
	v_pk_add_f32 v[106:107], v[106:107], v[110:111]
	s_nop 0
	v_pk_add_f32 v[70:71], v[70:71], v[106:107]
	s_nop 0
	v_add_f32_e32 v70, v70, v71
	s_waitcnt lgkmcnt(0)
	s_nop 1
	v_add_f32_dpp v70, v70, v70 quad_perm:[1,0,3,2] row_mask:0xf bank_mask:0xf
	s_nop 1
	v_add_f32_dpp v70, v70, v70 quad_perm:[2,3,0,1] row_mask:0xf bank_mask:0xf
	s_nop 1
	v_add_f32_dpp v70, v70, v70 row_half_mirror row_mask:0xf bank_mask:0xf
	s_nop 1
	v_add_f32_dpp v70, v70, v70 row_mirror row_mask:0xf bank_mask:0xf
	s_nop 1
	v_readlane_b32 s98, v70, 0
	v_readlane_b32 s99, v70, 16
	v_readlane_b32 s100, v70, 32
	v_readlane_b32 s101, v70, 48
	s_nop 1
	v_mov_b32_e32 v71, s99
	v_add_f32_e32 v71, s98, v71
	v_mov_b32_e32 v70, s101
	v_add_f32_e32 v70, s100, v70
	v_add_f32_e32 v70, v71, v70
	v_fmamk_f32 v70, v70, 0x3a800000, v241
	v_cmp_gt_f32_e32 vcc, s0, v70
	v_mul_f32_e32 v71, 0x4f800000, v70
	s_nop 0
	v_cndmask_b32_e32 v70, v70, v71, vcc
	v_sqrt_f32_e32 v71, v70
	s_nop 0
	v_add_u32_e32 v106, -1, v71
	v_fma_f32 v107, -v106, v71, v70
	v_cmp_ge_f32_e64 s[0:1], 0, v107
	v_add_u32_e32 v107, 1, v71
	s_nop 0
	v_cndmask_b32_e64 v106, v71, v106, s[0:1]
	v_fma_f32 v71, -v107, v71, v70
	v_cmp_lt_f32_e64 s[0:1], 0, v71
	s_nop 1
	v_cndmask_b32_e64 v71, v106, v107, s[0:1]
	v_mul_f32_e32 v106, 0x37800000, v71
	v_cndmask_b32_e32 v71, v71, v106, vcc
	v_cmp_class_f32_e32 vcc, v70, v188
	s_nop 1
	v_cndmask_b32_e32 v70, v71, v70, vcc
	v_div_scale_f32 v71, s[0:1], v70, v70, 1.0
	v_rcp_f32_e32 v106, v71
	s_nop 0
	v_fma_f32 v107, -v71, v106, 1.0
	v_fmac_f32_e32 v106, v107, v106
	v_div_scale_f32 v107, vcc, 1.0, v70, 1.0
	v_mul_f32_e32 v110, v107, v106
	v_fma_f32 v111, -v71, v110, v107
	v_fmac_f32_e32 v110, v111, v106
	v_fma_f32 v71, -v71, v110, v107
	v_div_fmas_f32 v71, v71, v106, v110
	v_div_fixup_f32 v110, v71, v70, 1.0
	v_pk_mul_f32 v[70:71], v[96:97], v[110:111] op_sel_hi:[1,0]
	v_pk_add_f32 v[106:107], v[20:21], 1.0 op_sel_hi:[1,0]
	v_pk_mul_f32 v[70:71], v[16:17], v[70:71]
	v_pk_mul_f32 v[96:97], v[108:109], v[110:111] op_sel_hi:[1,0]
	v_pk_fma_f32 v[106:107], v[106:107], v[70:71], v[40:41]
	v_pk_mul_f32 v[68:69], v[68:69], v[110:111] op_sel_hi:[1,0]
	v_pk_mul_f32 v[70:71], v[94:95], v[110:111] op_sel_hi:[1,0]
	v_pk_mul_f32 v[96:97], v[14:15], v[96:97]
	v_pk_add_f32 v[108:109], v[18:19], 1.0 op_sel_hi:[1,0]
	v_pk_mul_f32 v[94:95], v[10:11], v[70:71]
	v_pk_mul_f32 v[68:69], v[12:13], v[68:69]
	v_pk_add_f32 v[70:71], v[24:25], 1.0 op_sel_hi:[1,0]
	v_pk_fma_f32 v[108:109], v[108:109], v[96:97], v[38:39]
	v_pk_add_f32 v[96:97], v[22:23], 1.0 op_sel_hi:[1,0]
	v_pk_fma_f32 v[70:71], v[70:71], v[68:69], v[36:37]
	v_pk_mul_f32 v[68:69], v[102:103], v[110:111] op_sel_hi:[1,0]
	v_pk_fma_f32 v[96:97], v[96:97], v[94:95], v[34:35]
	v_pk_mul_f32 v[94:95], v[104:105], v[110:111] op_sel_hi:[1,0]
	v_pk_mul_f32 v[68:69], v[8:9], v[68:69]
	v_pk_add_f32 v[102:103], v[32:33], 1.0 op_sel_hi:[1,0]
	v_pk_mul_f32 v[98:99], v[98:99], v[110:111] op_sel_hi:[1,0]
	v_pk_mul_f32 v[94:95], v[6:7], v[94:95]
	v_pk_add_f32 v[104:105], v[30:31], 1.0 op_sel_hi:[1,0]
	v_pk_fma_f32 v[68:69], v[102:103], v[68:69], v[44:45]
	v_pk_mul_f32 v[100:101], v[100:101], v[110:111] op_sel_hi:[1,0]
	v_pk_mul_f32 v[98:99], v[4:5], v[98:99]
	v_pk_add_f32 v[102:103], v[28:29], 1.0 op_sel_hi:[1,0]
	v_pk_fma_f32 v[94:95], v[104:105], v[94:95], v[42:43]
	v_pk_mul_f32 v[100:101], v[2:3], v[100:101]
	v_pk_add_f32 v[104:105], v[26:27], 1.0 op_sel_hi:[1,0]
	v_pk_fma_f32 v[98:99], v[102:103], v[98:99], v[48:49]
	v_max_f32_e64 v102, |v108|, |v109|
	v_max_f32_e64 v103, |v106|, |v107|
	v_pk_fma_f32 v[100:101], v[104:105], v[100:101], v[46:47]
	v_max3_f32 v102, v102, 0, v103
	v_max_f32_e64 v103, |v96|, |v97|
	v_max_f32_e64 v104, |v70|, |v71|
	v_max3_f32 v102, v102, v103, v104
	v_max_f32_e64 v103, |v94|, |v95|
	v_max_f32_e64 v104, |v68|, |v69|
	v_max3_f32 v102, v102, v103, v104
	v_max_f32_e64 v103, |v100|, |v101|
	v_max_f32_e64 v104, |v98|, |v99|
	v_max3_f32 v102, v102, v103, v104
	s_waitcnt lgkmcnt(0)
	s_nop 1
	v_max_f32_dpp v102, v102, v102 quad_perm:[1,0,3,2] row_mask:0xf bank_mask:0xf
	s_nop 1
	v_max_f32_dpp v102, v102, v102 quad_perm:[2,3,0,1] row_mask:0xf bank_mask:0xf
	s_nop 1
	v_max_f32_dpp v102, v102, v102 row_half_mirror row_mask:0xf bank_mask:0xf
	s_nop 1
	v_max_f32_dpp v102, v102, v102 row_mirror row_mask:0xf bank_mask:0xf
	s_nop 1
	v_readlane_b32 s98, v102, 0
	v_readlane_b32 s99, v102, 16
	v_readlane_b32 s100, v102, 32
	v_readlane_b32 s101, v102, 48
	s_nop 1
	v_mov_b32_e32 v103, s99
	v_max_f32_e32 v103, s98, v103
	v_mov_b32_e32 v102, s101
	v_max_f32_e32 v102, s100, v102
	v_max_f32_e32 v104, v103, v102
	v_div_scale_f32 v102, s[10:11], v104, v104, s3
	v_rcp_f32_e32 v103, v102
	v_cmp_lt_f32_e64 s[0:1], 0, v104
	v_fma_f32 v105, -v102, v103, 1.0
	v_fmac_f32_e32 v103, v105, v103
	v_div_scale_f32 v105, vcc, s3, v104, s3
	v_mul_f32_e32 v110, v105, v103
	v_fma_f32 v111, -v102, v110, v105
	v_fmac_f32_e32 v110, v111, v103
	v_fma_f32 v102, -v102, v110, v105
	v_div_fmas_f32 v102, v102, v103, v110
	v_div_fixup_f32 v102, v102, v104, s3
	v_cndmask_b32_e64 v105, 0, v102, s[0:1]
	v_mul_f32_e32 v97, v97, v105
	v_mul_f32_e32 v96, v96, v105
	v_rndne_f32_e32 v97, v97
	v_mul_f32_e32 v70, v70, v105
	v_mul_f32_e32 v71, v71, v105
	v_rndne_f32_e32 v96, v96
	v_cvt_i32_f32_e32 v97, v97
	v_rndne_f32_e32 v70, v70
	v_rndne_f32_e32 v71, v71
	v_cvt_i32_f32_e32 v96, v96
	v_cvt_i32_f32_sdwa v70, v70 dst_sel:WORD_1 dst_unused:UNUSED_PAD src0_sel:DWORD
	v_cvt_i32_f32_e32 v71, v71
	v_lshl_add_u64 v[102:103], s[46:47], 0, v[90:91]
	s_mov_b32 s0, 0x40c0c00
	s_mov_b32 s1, 0x8900000
	v_lshlrev_b32_e32 v97, 8, v97
	v_add_co_u32_e32 v102, vcc, s1, v102
	v_and_b32_e32 v97, 0xff00, v97
	v_and_b32_e32 v70, 0xff0000, v70
	v_perm_b32 v71, v71, v96, s0
	v_addc_co_u32_e32 v103, vcc, 0, v103, vcc
	v_or3_b32 v70, v71, v97, v70
	v_mul_f32_e32 v71, v95, v105
	global_store_dword v[102:103], v70, off offset:256
	v_mul_f32_e32 v70, v94, v105
	v_rndne_f32_e32 v71, v71
	v_mul_f32_e32 v68, v68, v105
	v_mul_f32_e32 v69, v69, v105
	v_rndne_f32_e32 v70, v70
	v_cvt_i32_f32_e32 v71, v71
	v_rndne_f32_e32 v68, v68
	v_rndne_f32_e32 v69, v69
	v_cvt_i32_f32_e32 v70, v70
	v_cvt_i32_f32_sdwa v68, v68 dst_sel:WORD_1 dst_unused:UNUSED_PAD src0_sel:DWORD
	v_cvt_i32_f32_e32 v69, v69
	v_lshlrev_b32_e32 v71, 8, v71
	v_and_b32_e32 v71, 0xff00, v71
	v_and_b32_e32 v68, 0xff0000, v68
	v_perm_b32 v69, v69, v70, s0
	v_mul_f32_e32 v109, v109, v105
	v_or3_b32 v68, v69, v71, v68
	v_mul_f32_e32 v69, v101, v105
	v_mul_f32_e32 v108, v108, v105
	v_rndne_f32_e32 v109, v109
	v_mul_f32_e32 v106, v106, v105
	v_mul_f32_e32 v107, v107, v105
	global_store_dword v[102:103], v68, off offset:512
	v_mul_f32_e32 v68, v100, v105
	v_rndne_f32_e32 v69, v69
	v_mul_f32_e32 v70, v98, v105
	v_mul_f32_e32 v71, v99, v105
	v_rndne_f32_e32 v108, v108
	v_cvt_i32_f32_e32 v109, v109
	v_rndne_f32_e32 v106, v106
	v_rndne_f32_e32 v107, v107
	v_rndne_f32_e32 v68, v68
	v_cvt_i32_f32_e32 v69, v69
	v_rndne_f32_e32 v70, v70
	v_rndne_f32_e32 v71, v71
	v_cvt_i32_f32_e32 v108, v108
	v_cvt_i32_f32_sdwa v106, v106 dst_sel:WORD_1 dst_unused:UNUSED_PAD src0_sel:DWORD
	v_cvt_i32_f32_e32 v107, v107
	v_cvt_i32_f32_e32 v68, v68
	v_cvt_i32_f32_sdwa v70, v70 dst_sel:WORD_1 dst_unused:UNUSED_PAD src0_sel:DWORD
	v_cvt_i32_f32_e32 v71, v71
	v_lshlrev_b32_e32 v109, 8, v109
	v_lshlrev_b32_e32 v69, 8, v69
	v_and_b32_e32 v109, 0xff00, v109
	v_and_b32_e32 v106, 0xff0000, v106
	v_perm_b32 v107, v107, v108, s0
	v_and_b32_e32 v69, 0xff00, v69
	v_and_b32_e32 v70, 0xff0000, v70
	v_perm_b32 v68, v71, v68, s0
	v_or3_b32 v106, v107, v109, v106
	v_or3_b32 v68, v68, v69, v70
	global_store_dword v[102:103], v106, off
	global_store_dword v[102:103], v68, off offset:768
	s_and_saveexec_b64 s[0:1], s[36:37]
	s_cbranch_execz .LBB0_396
	v_readlane_b32 s40, v251, 5
	v_readlane_b32 s46, v251, 11
	v_readlane_b32 s47, v251, 12
	v_mul_f32_e32 v70, 0x3c010204, v104
	v_readlane_b32 s41, v251, 6
	v_lshl_add_u64 v[68:69], s[46:47], 0, v[92:93]
	v_readlane_b32 s42, v251, 7
	v_readlane_b32 s43, v251, 8
	v_readlane_b32 s44, v251, 9
	v_readlane_b32 s45, v251, 10
	global_store_dword v[68:69], v70, off
	s_branch .LBB0_396
